# m24 plus removal of 41 canonicalising max(x,x) / x+0 ops hipcc left in the attention softmax loops
# speedup vs baseline: 1.0023x; 1.0006x over previous
.LBB0_996:
	v_add_u32_e32 v202, s0, v221
	ds_read_b64_tr_b16 v[176:177], v202 offset:24576
	ds_read_b64_tr_b16 v[178:179], v202 offset:25088
	s_waitcnt lgkmcnt(9)
	v_mfma_f32_32x32x16_bf16 v[96:111], v[172:175], v[140:143], v[32:47]
	v_add_f32_e32 v80, v64, v65
	v_add_f32_e32 v80, v66, v80
	v_add_f32_e32 v80, v67, v80
	v_add_f32_e32 v80, v68, v80
	v_add_f32_e32 v80, v69, v80
	v_cvt_pk_bf16_f32 v132, v64, v65
	v_cvt_pk_bf16_f32 v133, v66, v67
	ds_read_b64_tr_b16 v[172:173], v202 offset:28672
	ds_read_b64_tr_b16 v[174:175], v202 offset:29184
	v_add_f32_e32 v64, v70, v80
	s_waitcnt lgkmcnt(10)
	v_mfma_f32_32x32x16_bf16 v[80:95], v[168:171], v[140:143], v[32:47]
	v_add_f32_e32 v64, v71, v64
	v_add_f32_e32 v64, v72, v64
	v_add_f32_e32 v112, v73, v64
	v_cvt_pk_bf16_f32 v134, v68, v69
	v_cvt_pk_bf16_f32 v135, v70, v71
	ds_read_b64_tr_b16 v[64:65], v202 offset:25600
	ds_read_b64_tr_b16 v[66:67], v202 offset:26112
	s_waitcnt lgkmcnt(11)
	v_mfma_f32_32x32x16_bf16 v[96:111], v[164:167], v[136:139], v[96:111]
	v_add_f32_e32 v68, v74, v112
	v_add_f32_e32 v68, v75, v68
	v_add_f32_e32 v68, v76, v68
	v_add_f32_e32 v112, v77, v68
	v_cvt_pk_bf16_f32 v128, v72, v73
	v_cvt_pk_bf16_f32 v129, v74, v75
	ds_read_b64_tr_b16 v[68:69], v202 offset:29696
	ds_read_b64_tr_b16 v[70:71], v202 offset:30208
	s_waitcnt lgkmcnt(12)
	v_mfma_f32_32x32x16_bf16 v[80:95], v[160:163], v[136:139], v[80:95]
	v_add_f32_e32 v72, v78, v112
	v_add_f32_e32 v72, v79, v72
	v_add_f32_e32 v72, v48, v72
	v_add_f32_e32 v112, v49, v72
	v_cvt_pk_bf16_f32 v130, v76, v77
	v_cvt_pk_bf16_f32 v131, v78, v79
	ds_read_b64_tr_b16 v[72:73], v202 offset:26624
	ds_read_b64_tr_b16 v[74:75], v202 offset:27136
	s_waitcnt lgkmcnt(13)
	v_mfma_f32_32x32x16_bf16 v[96:111], v[156:159], v[124:127], v[96:111]
	v_add_f32_e32 v76, v50, v112
	v_add_f32_e32 v76, v51, v76
	v_add_f32_e32 v76, v52, v76
	v_add_f32_e32 v76, v53, v76
	v_cvt_pk_bf16_f32 v116, v48, v49
	v_cvt_pk_bf16_f32 v117, v50, v51
	ds_read_b64_tr_b16 v[48:49], v202 offset:30720
	ds_read_b64_tr_b16 v[50:51], v202 offset:31232
	s_waitcnt lgkmcnt(14)
	v_mfma_f32_32x32x16_bf16 v[80:95], v[152:155], v[124:127], v[80:95]
	v_add_f32_e32 v76, v54, v76
	v_add_f32_e32 v76, v55, v76
	v_add_f32_e32 v76, v56, v76
	v_add_f32_e32 v76, v57, v76
	v_cvt_pk_bf16_f32 v118, v52, v53
	v_cvt_pk_bf16_f32 v119, v54, v55
	ds_read_b64_tr_b16 v[52:53], v202 offset:27648
	ds_read_b64_tr_b16 v[54:55], v202 offset:28160
	s_waitcnt lgkmcnt(14)
	v_mfma_f32_32x32x16_bf16 v[96:111], v[148:151], v[120:123], v[96:111]
	v_add_f32_e32 v76, v58, v76
	v_add_f32_e32 v76, v59, v76
	v_add_f32_e32 v76, v60, v76
	v_add_f32_e32 v76, v61, v76
	v_cvt_pk_bf16_f32 v112, v56, v57
	v_cvt_pk_bf16_f32 v113, v58, v59
	ds_read_b64_tr_b16 v[56:57], v202 offset:31744
	ds_read_b64_tr_b16 v[58:59], v202 offset:32256
	v_mfma_f32_32x32x16_bf16 v[80:95], v[144:147], v[120:123], v[80:95]
	v_add_f32_e32 v76, v62, v76
	v_add_f32_e32 v76, v63, v76
	v_cvt_pk_bf16_f32 v114, v60, v61
	v_cvt_pk_bf16_f32 v115, v62, v63
	v_lshl_add_u64 v[60:61], v[192:193], 0, s[30:31]
	s_add_i32 s0, s40, s47
	s_mov_b32 s1, m0
	s_mov_b32 m0, s0
	s_nop 0
	global_load_lds_dwordx4 v[60:61], off
	s_mov_b32 m0, s1
	v_lshl_add_u64 v[60:61], v[190:191], 0, s[30:31]
	s_add_i32 s0, s5, s52
	s_mov_b32 s1, m0
	s_mov_b32 m0, s0
	s_nop 0
	global_load_lds_dwordx4 v[60:61], off
	s_mov_b32 m0, s1
	v_max_f32_e32 v60, v96, v97
	v_max3_f32 v61, v98, v99, v81
	v_max3_f32 v60, v60, v80, v82
	v_max3_f32 v60, v60, v83, v100
	v_max3_f32 v61, v61, v102, v103
	v_max3_f32 v60, v60, v101, v84
	v_max3_f32 v61, v61, v86, v87
	v_max3_f32 v60, v60, v85, v104
	v_max3_f32 v61, v61, v106, v107
	v_max3_f32 v60, v60, v105, v88
	v_max3_f32 v61, v61, v90, v91
	v_max3_f32 v60, v60, v89, v108
	v_max3_f32 v61, v61, v110, v111
	v_max3_f32 v60, v60, v109, v92
	v_max3_f32 v61, v61, v94, v95
	v_max3_f32 v60, v60, v93, v61
	v_mov_b32_e32 v61, v60
	s_nop 1
	v_permlane32_swap_b32_e32 v60, v61
	v_max_f32_e32 v60, v60, v61
	v_cmp_lt_f32_e32 vcc, s33, v60
	s_cmp_lg_u64 vcc, 0
	v_add_f32_e32 v222, v222, v76
	s_cselect_b64 s[0:1], -1, 0
	s_cbranch_vccnz .LBB0_1004

.LBB0_999:
	s_add_i32 s0, s5, 0x2000
	s_cmpk_lg_i32 s5, 0x4000
	s_cselect_b32 s41, s0, 0
	v_add_u32_e32 v202, s40, v221
	ds_read_b64_tr_b16 v[148:149], v202 offset:24576
	ds_read_b64_tr_b16 v[150:151], v202 offset:25088
	s_waitcnt lgkmcnt(9)
	v_mfma_f32_32x32x16_bf16 v[64:79], v[60:63], v[140:143], v[32:47]
	v_add_f32_e32 v48, v96, v97
	v_add_f32_e32 v48, v98, v48
	v_add_f32_e32 v48, v99, v48
	v_add_f32_e32 v48, v100, v48
	v_add_f32_e32 v48, v101, v48
	v_cvt_pk_bf16_f32 v132, v96, v97
	v_cvt_pk_bf16_f32 v133, v98, v99
	ds_read_b64_tr_b16 v[144:145], v202 offset:28672
	ds_read_b64_tr_b16 v[146:147], v202 offset:29184
	v_add_f32_e32 v48, v102, v48
	v_add_f32_e32 v48, v103, v48
	v_add_f32_e32 v48, v104, v48
	v_add_f32_e32 v112, v105, v48
	s_waitcnt lgkmcnt(10)
	v_mfma_f32_32x32x16_bf16 v[48:63], v[172:175], v[140:143], v[32:47]
	v_cvt_pk_bf16_f32 v134, v100, v101
	v_cvt_pk_bf16_f32 v135, v102, v103
	ds_read_b64_tr_b16 v[96:97], v202 offset:25600
	ds_read_b64_tr_b16 v[98:99], v202 offset:26112
	s_waitcnt lgkmcnt(11)
	v_mfma_f32_32x32x16_bf16 v[64:79], v[176:179], v[136:139], v[64:79]
	v_add_f32_e32 v100, v106, v112
	v_add_f32_e32 v100, v107, v100
	v_add_f32_e32 v100, v108, v100
	v_add_f32_e32 v112, v109, v100
	v_cvt_pk_bf16_f32 v128, v104, v105
	v_cvt_pk_bf16_f32 v129, v106, v107
	ds_read_b64_tr_b16 v[100:101], v202 offset:29696
	ds_read_b64_tr_b16 v[102:103], v202 offset:30208
	s_waitcnt lgkmcnt(12)
	v_mfma_f32_32x32x16_bf16 v[48:63], v[168:171], v[136:139], v[48:63]
	v_add_f32_e32 v104, v110, v112
	v_add_f32_e32 v104, v111, v104
	v_add_f32_e32 v104, v80, v104
	v_add_f32_e32 v112, v81, v104
	v_cvt_pk_bf16_f32 v130, v108, v109
	v_cvt_pk_bf16_f32 v131, v110, v111
	ds_read_b64_tr_b16 v[104:105], v202 offset:26624
	ds_read_b64_tr_b16 v[106:107], v202 offset:27136
	s_waitcnt lgkmcnt(13)
	v_mfma_f32_32x32x16_bf16 v[64:79], v[164:167], v[124:127], v[64:79]
	v_add_f32_e32 v108, v82, v112
	v_add_f32_e32 v108, v83, v108
	v_add_f32_e32 v108, v84, v108
	v_add_f32_e32 v108, v85, v108
	v_cvt_pk_bf16_f32 v116, v80, v81
	v_cvt_pk_bf16_f32 v117, v82, v83
	ds_read_b64_tr_b16 v[80:81], v202 offset:30720
	ds_read_b64_tr_b16 v[82:83], v202 offset:31232
	s_waitcnt lgkmcnt(14)
	v_mfma_f32_32x32x16_bf16 v[48:63], v[160:163], v[124:127], v[48:63]
	v_add_f32_e32 v108, v86, v108
	v_add_f32_e32 v108, v87, v108
	v_add_f32_e32 v108, v88, v108
	v_add_f32_e32 v108, v89, v108
	v_cvt_pk_bf16_f32 v118, v84, v85
	v_cvt_pk_bf16_f32 v119, v86, v87
	ds_read_b64_tr_b16 v[84:85], v202 offset:27648
	ds_read_b64_tr_b16 v[86:87], v202 offset:28160
	s_waitcnt lgkmcnt(14)
	v_mfma_f32_32x32x16_bf16 v[64:79], v[156:159], v[120:123], v[64:79]
	v_add_f32_e32 v108, v90, v108
	v_add_f32_e32 v108, v91, v108
	v_add_f32_e32 v108, v92, v108
	v_add_f32_e32 v108, v93, v108
	v_cvt_pk_bf16_f32 v112, v88, v89
	v_cvt_pk_bf16_f32 v113, v90, v91
	ds_read_b64_tr_b16 v[88:89], v202 offset:31744
	ds_read_b64_tr_b16 v[90:91], v202 offset:32256
	v_mfma_f32_32x32x16_bf16 v[48:63], v[152:155], v[120:123], v[48:63]
	v_add_f32_e32 v108, v94, v108
	v_add_f32_e32 v108, v95, v108
	v_cvt_pk_bf16_f32 v114, v92, v93
	v_cvt_pk_bf16_f32 v115, v94, v95
	v_max_f32_e32 v92, v64, v65
	s_nop 3
	s_nop 2
	v_max3_f32 v93, v66, v67, v49
	v_max3_f32 v92, v92, v48, v50
	v_max3_f32 v92, v92, v51, v68
	v_max3_f32 v93, v93, v70, v71
	v_max3_f32 v92, v92, v69, v52
	v_max3_f32 v93, v93, v54, v55
	v_max3_f32 v92, v92, v53, v72
	v_max3_f32 v93, v93, v74, v75
	v_max3_f32 v92, v92, v73, v56
	v_max3_f32 v93, v93, v58, v59
	v_max3_f32 v92, v92, v57, v76
	v_max3_f32 v93, v93, v78, v79
	v_max3_f32 v92, v92, v77, v60
	v_max3_f32 v93, v93, v62, v63
	v_max3_f32 v92, v92, v61, v93
	v_mov_b32_e32 v93, v92
	s_nop 1
	v_permlane32_swap_b32_e32 v92, v93
	s_add_i32 s0, s5, s47
	s_mov_b32 s1, m0
	s_mov_b32 m0, s0
	s_nop 0
	global_load_lds_dwordx4 v[192:193], off
	s_mov_b32 m0, s1
	v_max_f32_e32 v92, v92, v93
	s_add_i32 s0, s41, s52
	s_mov_b32 s1, m0
	s_mov_b32 m0, s0
	s_nop 0
	global_load_lds_dwordx4 v[190:191], off
	s_mov_b32 m0, s1
	v_cmp_lt_f32_e32 vcc, s33, v92
	s_cmp_lg_u64 vcc, 0
	v_add_f32_e32 v222, v222, v108
	s_cselect_b64 s[0:1], -1, 0
	s_cbranch_vccnz .LBB0_1007

.LBB0_1011:
	v_add_u32_e32 v190, s0, v221
	ds_read_b64_tr_b16 v[176:177], v190 offset:24576
	ds_read_b64_tr_b16 v[178:179], v190 offset:25088
	s_waitcnt lgkmcnt(9)
	v_mfma_f32_32x32x16_bf16 v[96:111], v[172:175], v[140:143], v[32:47]
	v_add_f32_e32 v80, v64, v65
	v_add_f32_e32 v80, v66, v80
	v_add_f32_e32 v80, v67, v80
	v_add_f32_e32 v80, v68, v80
	v_add_f32_e32 v80, v69, v80
	v_cvt_pk_bf16_f32 v132, v64, v65
	v_cvt_pk_bf16_f32 v133, v66, v67
	ds_read_b64_tr_b16 v[172:173], v190 offset:28672
	ds_read_b64_tr_b16 v[174:175], v190 offset:29184
	v_add_f32_e32 v64, v70, v80
	s_waitcnt lgkmcnt(10)
	v_mfma_f32_32x32x16_bf16 v[80:95], v[168:171], v[140:143], v[32:47]
	v_add_f32_e32 v64, v71, v64
	v_add_f32_e32 v64, v72, v64
	v_add_f32_e32 v112, v73, v64
	v_cvt_pk_bf16_f32 v134, v68, v69
	v_cvt_pk_bf16_f32 v135, v70, v71
	ds_read_b64_tr_b16 v[64:65], v190 offset:25600
	ds_read_b64_tr_b16 v[66:67], v190 offset:26112
	s_waitcnt lgkmcnt(11)
	v_mfma_f32_32x32x16_bf16 v[96:111], v[164:167], v[136:139], v[96:111]
	v_add_f32_e32 v68, v74, v112
	v_add_f32_e32 v68, v75, v68
	v_add_f32_e32 v68, v76, v68
	v_add_f32_e32 v112, v77, v68
	v_cvt_pk_bf16_f32 v128, v72, v73
	v_cvt_pk_bf16_f32 v129, v74, v75
	ds_read_b64_tr_b16 v[68:69], v190 offset:29696
	ds_read_b64_tr_b16 v[70:71], v190 offset:30208
	s_waitcnt lgkmcnt(12)
	v_mfma_f32_32x32x16_bf16 v[80:95], v[160:163], v[136:139], v[80:95]
	v_add_f32_e32 v72, v78, v112
	v_add_f32_e32 v72, v79, v72
	v_add_f32_e32 v72, v48, v72
	v_add_f32_e32 v112, v49, v72
	v_cvt_pk_bf16_f32 v130, v76, v77
	v_cvt_pk_bf16_f32 v131, v78, v79
	ds_read_b64_tr_b16 v[72:73], v190 offset:26624
	ds_read_b64_tr_b16 v[74:75], v190 offset:27136
	s_waitcnt lgkmcnt(13)
	v_mfma_f32_32x32x16_bf16 v[96:111], v[156:159], v[124:127], v[96:111]
	v_add_f32_e32 v76, v50, v112
	v_add_f32_e32 v76, v51, v76
	v_add_f32_e32 v76, v52, v76
	v_add_f32_e32 v76, v53, v76
	v_cvt_pk_bf16_f32 v116, v48, v49
	v_cvt_pk_bf16_f32 v117, v50, v51
	ds_read_b64_tr_b16 v[48:49], v190 offset:30720
	ds_read_b64_tr_b16 v[50:51], v190 offset:31232
	s_waitcnt lgkmcnt(14)
	v_mfma_f32_32x32x16_bf16 v[80:95], v[152:155], v[124:127], v[80:95]
	v_add_f32_e32 v76, v54, v76
	v_add_f32_e32 v76, v55, v76
	v_add_f32_e32 v76, v56, v76
	v_add_f32_e32 v76, v57, v76
	v_cvt_pk_bf16_f32 v118, v52, v53
	v_cvt_pk_bf16_f32 v119, v54, v55
	ds_read_b64_tr_b16 v[52:53], v190 offset:27648
	ds_read_b64_tr_b16 v[54:55], v190 offset:28160
	s_waitcnt lgkmcnt(14)
	v_mfma_f32_32x32x16_bf16 v[96:111], v[148:151], v[120:123], v[96:111]
	v_add_f32_e32 v76, v58, v76
	v_add_f32_e32 v76, v59, v76
	v_add_f32_e32 v76, v60, v76
	v_add_f32_e32 v76, v61, v76
	v_cvt_pk_bf16_f32 v112, v56, v57
	v_cvt_pk_bf16_f32 v113, v58, v59
	ds_read_b64_tr_b16 v[56:57], v190 offset:31744
	ds_read_b64_tr_b16 v[58:59], v190 offset:32256
	v_mfma_f32_32x32x16_bf16 v[80:95], v[144:147], v[120:123], v[80:95]
	v_add_f32_e32 v76, v62, v76
	v_add_f32_e32 v76, v63, v76
	v_cvt_pk_bf16_f32 v114, v60, v61
	v_cvt_pk_bf16_f32 v115, v62, v63
	s_cmp_gt_u32 s53, 64
	s_cselect_b64 s[40:41], -1, 0
	s_and_b64 vcc, exec, s[40:41]
	s_cbranch_vccnz .LBB0_1013
	s_add_i32 s0, s55, s47
	v_lshl_add_u64 v[60:61], v[188:189], 0, s[38:39]
	s_mov_b32 s1, m0
	s_mov_b32 m0, s0
	s_nop 0
	global_load_lds_dwordx4 v[60:61], off
	s_mov_b32 m0, s1
.LBB0_1013:
	v_lshl_add_u64 v[190:191], v[184:185], 0, s[38:39]
	s_mov_b64 s[0:1], 0x100000
	v_lshl_add_u64 v[60:61], v[190:191], 0, s[0:1]
	s_add_i32 s0, s54, s52
	s_mov_b32 s1, m0
	s_mov_b32 m0, s0
	s_nop 0
	global_load_lds_dwordx4 v[60:61], off
	s_mov_b32 m0, s1
	v_max_f32_e32 v60, v96, v97
	v_max3_f32 v61, v98, v99, v81
	v_max3_f32 v60, v60, v80, v82
	v_max3_f32 v60, v60, v83, v100
	v_max3_f32 v61, v61, v102, v103
	v_max3_f32 v60, v60, v101, v84
	v_max3_f32 v61, v61, v86, v87
	v_max3_f32 v60, v60, v85, v104
	v_max3_f32 v61, v61, v106, v107
	v_max3_f32 v60, v60, v105, v88
	v_max3_f32 v61, v61, v90, v91
	v_max3_f32 v60, v60, v89, v108
	v_max3_f32 v61, v61, v110, v111
	v_max3_f32 v60, v60, v109, v92
	v_max3_f32 v61, v61, v94, v95
	v_max3_f32 v60, v60, v93, v61
	v_mov_b32_e32 v61, v60
	s_nop 1
	v_permlane32_swap_b32_e32 v60, v61
	v_max_f32_e32 v60, v60, v61
	v_cmp_lt_f32_e32 vcc, s33, v60
	s_cmp_lg_u64 vcc, 0
	v_add_f32_e32 v192, v222, v76
	s_cselect_b64 s[0:1], -1, 0
	s_cbranch_vccnz .LBB0_1039

.LBB0_1018:
	v_add_u32_e32 v193, s55, v221
	ds_read_b64_tr_b16 v[152:153], v193 offset:24576
	ds_read_b64_tr_b16 v[154:155], v193 offset:25088
	s_waitcnt lgkmcnt(9)
	v_mfma_f32_32x32x16_bf16 v[64:79], v[60:63], v[140:143], v[32:47]
	v_add_f32_e32 v48, v96, v97
	v_add_f32_e32 v48, v98, v48
	v_add_f32_e32 v48, v99, v48
	v_add_f32_e32 v48, v100, v48
	v_add_f32_e32 v48, v101, v48
	v_cvt_pk_bf16_f32 v132, v96, v97
	v_cvt_pk_bf16_f32 v133, v98, v99
	ds_read_b64_tr_b16 v[148:149], v193 offset:28672
	ds_read_b64_tr_b16 v[150:151], v193 offset:29184
	v_add_f32_e32 v48, v102, v48
	v_add_f32_e32 v48, v103, v48
	v_add_f32_e32 v48, v104, v48
	v_add_f32_e32 v112, v105, v48
	s_waitcnt lgkmcnt(10)
	v_mfma_f32_32x32x16_bf16 v[48:63], v[172:175], v[140:143], v[32:47]
	v_cvt_pk_bf16_f32 v134, v100, v101
	v_cvt_pk_bf16_f32 v135, v102, v103
	ds_read_b64_tr_b16 v[96:97], v193 offset:25600
	ds_read_b64_tr_b16 v[98:99], v193 offset:26112
	s_waitcnt lgkmcnt(11)
	v_mfma_f32_32x32x16_bf16 v[64:79], v[176:179], v[136:139], v[64:79]
	v_add_f32_e32 v100, v106, v112
	v_add_f32_e32 v100, v107, v100
	v_add_f32_e32 v100, v108, v100
	v_add_f32_e32 v112, v109, v100
	v_cvt_pk_bf16_f32 v128, v104, v105
	v_cvt_pk_bf16_f32 v129, v106, v107
	ds_read_b64_tr_b16 v[100:101], v193 offset:29696
	ds_read_b64_tr_b16 v[102:103], v193 offset:30208
	s_waitcnt lgkmcnt(12)
	v_mfma_f32_32x32x16_bf16 v[48:63], v[168:171], v[136:139], v[48:63]
	v_add_f32_e32 v104, v110, v112
	v_add_f32_e32 v104, v111, v104
	v_add_f32_e32 v104, v80, v104
	v_add_f32_e32 v112, v81, v104
	v_cvt_pk_bf16_f32 v130, v108, v109
	v_cvt_pk_bf16_f32 v131, v110, v111
	ds_read_b64_tr_b16 v[104:105], v193 offset:26624
	ds_read_b64_tr_b16 v[106:107], v193 offset:27136
	s_waitcnt lgkmcnt(13)
	v_mfma_f32_32x32x16_bf16 v[64:79], v[164:167], v[124:127], v[64:79]
	v_add_f32_e32 v108, v82, v112
	v_add_f32_e32 v108, v83, v108
	v_add_f32_e32 v108, v84, v108
	v_add_f32_e32 v108, v85, v108
	v_cvt_pk_bf16_f32 v116, v80, v81
	v_cvt_pk_bf16_f32 v117, v82, v83
	ds_read_b64_tr_b16 v[80:81], v193 offset:30720
	ds_read_b64_tr_b16 v[82:83], v193 offset:31232
	s_waitcnt lgkmcnt(14)
	v_mfma_f32_32x32x16_bf16 v[48:63], v[160:163], v[124:127], v[48:63]
	v_add_f32_e32 v108, v86, v108
	v_add_f32_e32 v108, v87, v108
	v_add_f32_e32 v108, v88, v108
	v_add_f32_e32 v108, v89, v108
	v_cvt_pk_bf16_f32 v118, v84, v85
	v_cvt_pk_bf16_f32 v119, v86, v87
	ds_read_b64_tr_b16 v[84:85], v193 offset:27648
	ds_read_b64_tr_b16 v[86:87], v193 offset:28160
	s_waitcnt lgkmcnt(14)
	v_mfma_f32_32x32x16_bf16 v[64:79], v[156:159], v[120:123], v[64:79]
	v_add_f32_e32 v108, v90, v108
	v_add_f32_e32 v108, v91, v108
	v_add_f32_e32 v108, v92, v108
	v_add_f32_e32 v108, v93, v108
	v_cvt_pk_bf16_f32 v112, v88, v89
	v_cvt_pk_bf16_f32 v113, v90, v91
	ds_read_b64_tr_b16 v[88:89], v193 offset:31744
	ds_read_b64_tr_b16 v[90:91], v193 offset:32256
	v_mfma_f32_32x32x16_bf16 v[48:63], v[144:147], v[120:123], v[48:63]
	v_add_f32_e32 v108, v94, v108
	v_add_f32_e32 v108, v95, v108
	v_cvt_pk_bf16_f32 v114, v92, v93
	v_cvt_pk_bf16_f32 v115, v94, v95
	s_cmp_gt_u32 s53, 63
	s_cselect_b64 s[0:1], -1, 0
	s_and_b64 vcc, exec, s[0:1]
	s_cbranch_vccnz .LBB0_1020
	v_lshl_add_u64 v[92:93], v[186:187], 0, s[38:39]
	s_mov_b64 s[2:3], 0x10000
	s_add_i32 s4, s54, s47
	v_lshl_add_u64 v[92:93], v[92:93], 0, s[2:3]
	s_mov_b32 s2, m0
	s_mov_b32 m0, s4
	s_nop 0
	global_load_lds_dwordx4 v[92:93], off
	s_mov_b32 m0, s2
.LBB0_1020:
	s_add_i32 s2, s54, 0x2000
	s_cmpk_lg_i32 s54, 0x4000
	s_cselect_b32 s55, s2, 0
	v_lshl_add_u64 v[92:93], v[190:191], 0, s[34:35]
	s_add_i32 s2, s55, s52
	s_mov_b32 s3, m0
	s_mov_b32 m0, s2
	s_nop 0
	global_load_lds_dwordx4 v[92:93], off
	s_mov_b32 m0, s3
	v_max_f32_e32 v92, v64, v65
	v_max3_f32 v93, v66, v67, v49
	v_max3_f32 v92, v92, v48, v50
	v_max3_f32 v92, v92, v51, v68
	v_max3_f32 v93, v93, v70, v71
	v_max3_f32 v92, v92, v69, v52
	v_max3_f32 v93, v93, v54, v55
	v_max3_f32 v92, v92, v53, v72
	v_max3_f32 v93, v93, v74, v75
	v_max3_f32 v92, v92, v73, v56
	v_max3_f32 v93, v93, v58, v59
	v_max3_f32 v92, v92, v57, v76
	v_max3_f32 v93, v93, v78, v79
	v_max3_f32 v92, v92, v77, v60
	v_max3_f32 v93, v93, v62, v63
	v_max3_f32 v92, v92, v61, v93
	v_mov_b32_e32 v93, v92
	s_nop 1
	v_permlane32_swap_b32_e32 v92, v93
	v_max_f32_e32 v92, v92, v93
	v_cmp_lt_f32_e32 vcc, s33, v92
	s_cmp_lg_u64 vcc, 0
	v_add_f32_e32 v222, v192, v108
	s_cselect_b64 s[2:3], -1, 0
	s_cbranch_vccnz .LBB0_1042

;   #define RESC() do{ if(resc){ asm volatile("s_waitcnt lgkmcnt(0)":::"memory"); \
;       _Pragma("unroll") for(int d_=0;d_<2;++d_) _Pragma("unroll") for(int r=0;r<16;++r)o[d_][r]*=wsf[crow(r,hi)]; } }while(0)
; template<int THRL> __device__ __forceinline__ void attn_unit(long qrow0,int qcol,long kvrow0,int kvcol,int NT,long orow0,int ocol,const bf16*Q,const bf16* K,const bf16* V,bf16*O,char*shm,int wave_){
;     ...
;   STEP(pB0,pB1,pA0,pA1,NT-1,false,false,false); RESC();
.LBB0_1045:
	ds_read_b64_tr_b16 v[96:97], v221 offset:24576
	ds_read_b64_tr_b16 v[98:99], v221 offset:25088
	v_add_f32_e32 v80, v64, v65
	v_add_f32_e32 v80, v66, v80
	v_add_f32_e32 v80, v67, v80
	v_add_f32_e32 v80, v68, v80
	v_add_f32_e32 v100, v69, v80
	s_waitcnt lgkmcnt(9)
	v_mfma_f32_32x32x16_bf16 v[80:95], v[172:175], v[140:143], v[32:47]
	v_cvt_pk_bf16_f32 v132, v64, v65
	v_cvt_pk_bf16_f32 v133, v66, v67
	ds_read_b64_tr_b16 v[64:65], v221 offset:28672
	ds_read_b64_tr_b16 v[66:67], v221 offset:29184
	s_waitcnt lgkmcnt(10)
	v_mfma_f32_32x32x16_bf16 v[32:47], v[168:171], v[140:143], v[32:47]
	v_add_f32_e32 v100, v70, v100
	v_add_f32_e32 v100, v71, v100
	v_add_f32_e32 v100, v72, v100
	v_add_f32_e32 v100, v73, v100
	v_cvt_pk_bf16_f32 v134, v68, v69
	v_cvt_pk_bf16_f32 v135, v70, v71
	ds_read_b64_tr_b16 v[68:69], v221 offset:25600
	ds_read_b64_tr_b16 v[70:71], v221 offset:26112
	s_waitcnt lgkmcnt(11)
	v_mfma_f32_32x32x16_bf16 v[80:95], v[164:167], v[136:139], v[80:95]
	v_add_f32_e32 v100, v74, v100
	v_add_f32_e32 v100, v75, v100
	v_add_f32_e32 v100, v76, v100
	v_add_f32_e32 v100, v77, v100
	v_cvt_pk_bf16_f32 v128, v72, v73
	v_cvt_pk_bf16_f32 v129, v74, v75
	ds_read_b64_tr_b16 v[72:73], v221 offset:29696
	ds_read_b64_tr_b16 v[74:75], v221 offset:30208
	s_waitcnt lgkmcnt(12)
	v_mfma_f32_32x32x16_bf16 v[32:47], v[160:163], v[136:139], v[32:47]
	v_add_f32_e32 v100, v78, v100
	v_add_f32_e32 v100, v79, v100
	v_add_f32_e32 v100, v48, v100
	v_add_f32_e32 v100, v49, v100
	v_cvt_pk_bf16_f32 v130, v76, v77
	v_cvt_pk_bf16_f32 v131, v78, v79
	ds_read_b64_tr_b16 v[76:77], v221 offset:26624
	ds_read_b64_tr_b16 v[78:79], v221 offset:27136
	s_waitcnt lgkmcnt(13)
	v_mfma_f32_32x32x16_bf16 v[80:95], v[156:159], v[124:127], v[80:95]
	v_add_f32_e32 v100, v50, v100
	v_add_f32_e32 v100, v51, v100
	v_add_f32_e32 v100, v52, v100
	v_add_f32_e32 v104, v53, v100
	v_cvt_pk_bf16_f32 v116, v48, v49
	v_cvt_pk_bf16_f32 v117, v50, v51
	ds_read_b64_tr_b16 v[100:101], v221 offset:30720
	ds_read_b64_tr_b16 v[102:103], v221 offset:31232
	s_waitcnt lgkmcnt(14)
	v_mfma_f32_32x32x16_bf16 v[32:47], v[152:155], v[124:127], v[32:47]
	v_add_f32_e32 v48, v54, v104
	v_add_f32_e32 v48, v55, v48
	v_add_f32_e32 v48, v56, v48
	v_add_f32_e32 v48, v57, v48
	v_cvt_pk_bf16_f32 v118, v52, v53
	v_cvt_pk_bf16_f32 v119, v54, v55
	ds_read_b64_tr_b16 v[104:105], v221 offset:27648
	ds_read_b64_tr_b16 v[106:107], v221 offset:28160
	s_waitcnt lgkmcnt(14)
	v_mfma_f32_32x32x16_bf16 v[80:95], v[148:151], v[120:123], v[80:95]
	v_add_f32_e32 v48, v58, v48
	v_add_f32_e32 v48, v59, v48
	v_add_f32_e32 v48, v60, v48
	v_add_f32_e32 v48, v61, v48
	v_cvt_pk_bf16_f32 v112, v56, v57
	v_cvt_pk_bf16_f32 v113, v58, v59
	ds_read_b64_tr_b16 v[108:109], v221 offset:31744
	ds_read_b64_tr_b16 v[110:111], v221 offset:32256
	v_mfma_f32_32x32x16_bf16 v[32:47], v[144:147], v[120:123], v[32:47]
	v_add_f32_e32 v48, v62, v48
	v_add_f32_e32 v48, v63, v48
	v_cvt_pk_bf16_f32 v114, v60, v61
	v_cvt_pk_bf16_f32 v115, v62, v63
	v_max_f32_e32 v49, v80, v81
	s_nop 3
	s_nop 2
	v_max3_f32 v50, v82, v83, v33
	v_max3_f32 v49, v49, v32, v34
	v_max3_f32 v49, v49, v35, v84
	v_max3_f32 v50, v50, v86, v87
	v_max3_f32 v49, v49, v85, v36
	v_max3_f32 v50, v50, v38, v39
	v_max3_f32 v49, v49, v37, v88
	v_max3_f32 v50, v50, v90, v91
	v_max3_f32 v49, v49, v89, v40
	v_max3_f32 v50, v50, v42, v43
	v_max3_f32 v49, v49, v41, v92
	v_max3_f32 v50, v50, v94, v95
	v_max3_f32 v49, v49, v93, v44
	v_max3_f32 v50, v50, v46, v47
	v_add_f32_e32 v120, v222, v48
	v_max3_f32 v48, v49, v45, v50
	v_mov_b32_e32 v49, v48
	s_nop 1
	v_permlane32_swap_b32_e32 v48, v49
	v_max_f32_e32 v48, v48, v49
	v_cmp_lt_f32_e32 vcc, s33, v48
	s_cmp_lg_u64 vcc, 0
	s_cselect_b64 s[0:1], -1, 0
	s_cbranch_vccnz .LBB0_1050

.LBB0_1050:
	v_max_f32_e32 v121, 0, v48
	v_add_f32_e32 v48, v199, v121
	v_xor_b32_e32 v48, 0x80000000, v48
	v_mov_b32_e32 v49, v48
	v_mov_b32_e32 v50, v48
	v_mov_b32_e32 v51, v48
	v_mov_b32_e32 v52, v48
	v_mov_b32_e32 v53, v48
	v_mov_b32_e32 v54, v48
	v_mov_b32_e32 v55, v48
	v_mov_b32_e32 v56, v48
	v_mov_b32_e32 v57, v48
	v_mov_b32_e32 v58, v48
	v_mov_b32_e32 v59, v48
	v_mov_b32_e32 v60, v48
	v_mov_b32_e32 v61, v48
	v_mov_b32_e32 v62, v48
	v_mov_b32_e32 v63, v48
	s_nop 0
	v_exp_f32_e64 v48, -v121
	s_and_saveexec_b64 s[2:3], s[36:37]
	ds_write_b32 v220, v48 offset:49152
	s_or_b64 exec, exec, s[2:3]
	v_sub_f32_e32 v95, v95, v121
	v_sub_f32_e32 v94, v94, v121
	v_sub_f32_e32 v93, v93, v121
	v_sub_f32_e32 v92, v92, v121
	v_sub_f32_e32 v91, v91, v121
	v_sub_f32_e32 v90, v90, v121
	v_sub_f32_e32 v89, v89, v121
	v_sub_f32_e32 v88, v88, v121
	v_sub_f32_e32 v87, v87, v121
	v_sub_f32_e32 v86, v86, v121
	v_sub_f32_e32 v85, v85, v121
	v_sub_f32_e32 v84, v84, v121
	v_sub_f32_e32 v83, v83, v121
	v_sub_f32_e32 v82, v82, v121
	v_sub_f32_e32 v81, v81, v121
	v_sub_f32_e32 v80, v80, v121
	v_sub_f32_e32 v47, v47, v121
	v_sub_f32_e32 v46, v46, v121
	v_sub_f32_e32 v45, v45, v121
	v_sub_f32_e32 v44, v44, v121
	v_sub_f32_e32 v43, v43, v121
	v_sub_f32_e32 v42, v42, v121
	v_sub_f32_e32 v41, v41, v121
	v_sub_f32_e32 v40, v40, v121
	v_sub_f32_e32 v39, v39, v121
	v_sub_f32_e32 v38, v38, v121
	v_sub_f32_e32 v37, v37, v121
	v_sub_f32_e32 v36, v36, v121
	v_sub_f32_e32 v35, v35, v121
	v_sub_f32_e32 v34, v34, v121
	v_sub_f32_e32 v33, v33, v121
	v_sub_f32_e32 v32, v32, v121
	v_mul_f32_e32 v120, v120, v48
	s_branch .LBB0_1046

; #define WAIT_BAR(N) asm volatile("s_waitcnt vmcnt(" #N ") lgkmcnt(0)\n\ts_barrier":::"memory")
;   #define DMA_K(t,slot) glds16(ksrc+(long)(t)*KVBLK*KP,(unsigned)__builtin_amdgcn_readfirstlane(kdst+(slot)))
;   #define DMA_V(t,slot) glds16(vsrc+(long)(t)*KVBLK*KP,(unsigned)__builtin_amdgcn_readfirstlane(vdst+(slot)))
;   #define CMASK(P0,P1,t) do{}while(0)
; template<int THRL> __device__ __forceinline__ void attn_unit(long qrow0,int qcol,long kvrow0,int kvcol,int NT,long orow0,int ocol,const bf16*Q,const bf16* K,const bf16* V,bf16*O,char*shm,int wave_){
;   int lane_=(int)__builtin_amdgcn_mbcnt_hi(~0u,__builtin_amdgcn_mbcnt_lo(~0u,0u)); asm volatile("":"+s"(wave_),"+v"(lane_)); const int wid=wave_; const int lane=lane_,tid=wid*64+lane,r32=lane&31,hi=lane>>5;
;   const bf16*Qw=Q+(qrow0+wid*QBLK)*QP+qcol;
;   const bf16*Kh=K+kvrow0*KP+kvcol,*Vh=V+kvrow0*KP+kvcol;
;   const unsigned lds0=(unsigned)(uintptr_t)shm;
;   float*wsf=(float*)(shm+LDS_WS)+wid*64;
;   const bf16*ksrc=Kh+(long)lane*KP+wid*8;
;   const bf16*vsrc=Vh+(long)(16*(wid&3)+(lane>>2))*KP+(wid>>2)*32+(lane&3)*8;
;   const unsigned kdst=lds0+LDS_K+wid*1024, vdst=lds0+LDS_V+wid*1024;
;     ...
;   const int vb0=(int)(lds0+LDS_V)+((lane>>4)&1)*32+(lane&3)*8+(4*hi+((lane&15)>>2))*64;
;   const char*Kbase=shm+LDS_K; bf16x8 kf[8];
;   const lds_cptr shm3=(lds_cptr)shm; const lds_cptr kp0=shm3+LDS_K+hi*1024+r32*16; const lds_cptr vp0=shm3+LDS_V+((lane>>4)&1)*32+(lane&3)*8+(4*hi+((lane&15)>>2))*64;
;   DMA_K(0,0);DMA_V(0,0);DMA_K(1,SLOTB);
;   bf16x8 qr[4];
;   #pragma unroll
;   for(int d0=0;d0<4;++d0)qr[d0]=*reinterpret_cast<const bf16x8*>(&Qw[(long)r32*QP+d0*16+hi*8]);
;   float mhat=0.f,l_reg=0.f;f32x16 o[2];{float z_=0.f;asm volatile("":"+v"(z_));
;     _Pragma("unroll") for(int r=0;r<16;++r){o[0][r]=z_;o[1][r]=z_;}}f32x16 negm=o[0];asm volatile("":"+v"(negm));
;     ...
;   bool resc=false;
;     ...
;   f32x16 pA0,pA1,pB0,pB1;
;   int sl_prev=0,sl_cur=0,sl_next=SLOTB;
;     ...
;   DMA_K(2,2*SLOTB);
;   WAIT_BAR(3);
;   qkt(pA0,pA1,Kbase,qr,negm,r32,hi);asm volatile("s_nop 15\n\ts_nop 7":"+v"(pA0),"+v"(pA1));CMASK(pA0,pA1,0);
;   START(pA0,pA1);
.LBB0_1058:
	s_ashr_i32 s18, s4, 3
	v_mov_b32_e32 v182, v200
	s_mov_b32 s5, s6
	s_lshl_b32 s0, s18, 8
	s_lshl_b32 s2, s5, 5
	s_and_b32 s17, s4, 7
	s_ashr_i32 s1, s0, 31
	s_ashr_i32 s3, s2, 31
	s_add_u32 s0, s0, s2
	s_addc_u32 s1, s1, s3
	s_add_u32 s20, s0, 0x8000
	s_addc_u32 s21, s1, 0
	s_lshl_b64 s[0:1], s[20:21], 10
	s_add_u32 s0, s7, s0
	s_addc_u32 s1, s8, s1
	s_lshl_b32 s2, s17, 7
	s_add_u32 s2, s0, s2
	s_addc_u32 s3, s1, 0
	s_mul_hi_i32 s0, s18, 0x110000
	s_mul_i32 s18, s18, 0x110000
	s_add_u32 s18, s18, 0x100000
	s_addc_u32 s19, s0, 0
	s_add_u32 s0, s9, s18
	s_addc_u32 s1, s12, s19
	s_lshl_b32 s22, s4, 5
	s_and_b32 s22, s22, 0x80
	s_add_u32 s0, s0, s22
	s_addc_u32 s1, s1, 0
	s_add_u32 s18, s13, s18
	s_addc_u32 s19, s14, s19
	v_ashrrev_i32_e32 v183, 31, v182
	s_add_u32 s18, s18, s22
	v_lshlrev_b64 v[0:1], 8, v[182:183]
	s_addc_u32 s19, s19, 0
	v_lshl_add_u64 v[0:1], s[0:1], 0, v[0:1]
	s_lshl_b32 s0, s5, 3
	s_ashr_i32 s1, s0, 31
	v_lshl_add_u64 v[48:49], s[0:1], 1, v[0:1]
	s_lshl_b32 s1, s5, 4
	s_and_b32 s1, s1, 48
	v_ashrrev_i32_e32 v0, 2, v182
	v_add_u32_e32 v0, s1, v0
	v_ashrrev_i32_e32 v1, 31, v0
	v_lshlrev_b64 v[0:1], 8, v[0:1]
	s_andn2_b32 s0, s0, 31
	v_lshl_add_u64 v[0:1], s[18:19], 0, v[0:1]
	s_ashr_i32 s1, s0, 31
	v_lshl_add_u64 v[0:1], s[0:1], 1, v[0:1]
	s_lshl_b32 s0, s5, 10
	v_lshlrev_b32_e32 v183, 3, v182
	s_cmp_lg_u32 0, -1
	v_and_b32_e32 v187, 24, v183
	s_cselect_b32 s1, 0, 0
	v_lshlrev_b32_e32 v180, 1, v187
	s_add_i32 s0, s1, s0
	s_mov_b32 s1, m0
	s_mov_b32 m0, s0
	s_nop 0
	global_load_lds_dwordx4 v[48:49], off
	s_mov_b32 m0, s1
	s_mov_b64 s[22:23], 0x4000
	v_ashrrev_i32_e32 v144, 5, v182
	v_lshl_add_u64 v[184:185], v[0:1], 0, v[180:181]
	s_add_i32 s19, s0, 0x6000
	s_mov_b32 s1, m0
	s_mov_b32 m0, s19
	s_nop 0
	global_load_lds_dwordx4 v[184:185], off
	s_mov_b32 m0, s1
	v_lshl_add_u64 v[0:1], v[48:49], 0, s[22:23]
	s_add_i32 s1, s0, 0x2000
	s_mov_b32 s18, m0
	s_mov_b32 m0, s1
	s_nop 0
	global_load_lds_dwordx4 v[0:1], off
	s_mov_b32 m0, s18
	v_lshlrev_b32_e32 v0, 3, v144
	v_and_b32_e32 v186, 31, v182
	v_ashrrev_i32_e32 v1, 31, v0
	v_lshl_add_u64 v[0:1], v[0:1], 1, s[2:3]
	v_lshlrev_b32_e32 v180, 10, v186
	v_lshl_add_u64 v[2:3], v[0:1], 0, v[180:181]
	global_load_dwordx4 v[140:143], v[2:3], off
	global_load_dwordx4 v[136:139], v[2:3], off offset:32
	global_load_dwordx4 v[116:119], v[2:3], off offset:64
	global_load_dwordx4 v[112:115], v[2:3], off offset:96
	v_mov_b32_e32 v0, v181
	v_lshlrev_b32_e32 v1, 4, v186
	s_waitcnt vmcnt(4)
	v_lshl_add_u32 v4, v144, 10, 0
	v_add_u32_e32 v194, v4, v1
	v_mov_b32_e32 v14, v0
	v_mov_b32_e32 v15, v0
	v_mov_b32_e32 v1, v0
	v_mov_b32_e32 v2, v0
	v_mov_b32_e32 v3, v0
	v_mov_b32_e32 v4, v0
	v_mov_b32_e32 v5, v0
	v_mov_b32_e32 v6, v0
	v_mov_b32_e32 v7, v0
	v_mov_b32_e32 v8, v0
	v_mov_b32_e32 v9, v0
	v_mov_b32_e32 v10, v0
	v_mov_b32_e32 v11, v0
	v_mov_b32_e32 v12, v0
	v_mov_b32_e32 v13, v0
	v_mov_b64_e32 v[30:31], v[14:15]
	v_mov_b64_e32 v[28:29], v[12:13]
	v_mov_b64_e32 v[26:27], v[10:11]
	v_mov_b64_e32 v[24:25], v[8:9]
	v_mov_b64_e32 v[22:23], v[6:7]
	v_mov_b64_e32 v[20:21], v[4:5]
	v_mov_b64_e32 v[18:19], v[2:3]
	v_mov_b64_e32 v[16:17], v[0:1]
	v_lshl_add_u64 v[32:33], v[48:49], 0, s[10:11]
	s_add_i32 s1, s0, 0x4000
	s_mov_b32 s2, m0
	s_mov_b32 m0, s1
	s_nop 0
	global_load_lds_dwordx4 v[32:33], off
	s_mov_b32 m0, s2
	s_waitcnt vmcnt(3) lgkmcnt(0)
	s_barrier
	ds_read_b128 v[50:53], v194
	ds_read_b128 v[54:57], v194 offset:512
	v_lshlrev_b32_e32 v180, 8, v144
	s_movk_i32 s1, 0xc0
	s_mov_b64 s[2:3], 0xc000
	v_cmp_gt_u32_e64 s[36:37], 32, v182
	s_waitcnt vmcnt(3) lgkmcnt(1)
	v_mfma_f32_32x32x16_bf16 v[32:47], v[50:53], v[140:143], v[16:31]
	s_waitcnt lgkmcnt(0)
	v_mfma_f32_32x32x16_bf16 v[16:31], v[54:57], v[140:143], v[16:31]
	ds_read_b128 v[50:53], v194 offset:2048
	ds_read_b128 v[54:57], v194 offset:2560
	s_waitcnt vmcnt(2) lgkmcnt(1)
	v_mfma_f32_32x32x16_bf16 v[32:47], v[50:53], v[136:139], v[32:47]
	s_waitcnt lgkmcnt(0)
	v_mfma_f32_32x32x16_bf16 v[16:31], v[54:57], v[136:139], v[16:31]
	ds_read_b128 v[50:53], v194 offset:4096
	ds_read_b128 v[54:57], v194 offset:4608
	s_waitcnt vmcnt(1) lgkmcnt(1)
	v_mfma_f32_32x32x16_bf16 v[32:47], v[50:53], v[116:119], v[32:47]
	s_waitcnt lgkmcnt(0)
	v_mfma_f32_32x32x16_bf16 v[16:31], v[54:57], v[116:119], v[16:31]
	ds_read_b128 v[50:53], v194 offset:6144
	ds_read_b128 v[54:57], v194 offset:6656
	s_waitcnt vmcnt(0) lgkmcnt(1)
	v_mfma_f32_32x32x16_bf16 v[32:47], v[50:53], v[112:115], v[32:47]
	v_lshlrev_b32_e32 v51, 4, v182
	v_and_or_b32 v189, v51, s1, v180
	s_lshl_b32 s1, s5, 8
	s_add_i32 s18, s1, 0
	v_lshlrev_b32_e32 v50, 1, v182
	v_and_b32_e32 v188, 32, v50
	v_add3_u32 v50, 0, v188, v187
	s_waitcnt lgkmcnt(0)
	v_mfma_f32_32x32x16_bf16 v[16:31], v[54:57], v[112:115], v[16:31]
	s_nop 15
	s_nop 7
	v_add_u32_e32 v193, v50, v189
	v_max3_f32 v51, v32, v33, v16
	v_max3_f32 v52, v34, v35, v17
	v_lshl_add_u32 v192, v186, 2, s18
	v_max3_f32 v51, v51, v18, v19
	v_max3_f32 v52, v52, v38, v39
	s_nop 0
	v_max3_f32 v51, v51, v36, v37
	v_max3_f32 v52, v52, v22, v23
	s_nop 0
	v_max3_f32 v51, v51, v20, v21
	v_max3_f32 v52, v52, v42, v43
	s_nop 0
	v_max3_f32 v51, v51, v40, v41
	v_max3_f32 v52, v52, v26, v27
	s_nop 0
	v_max3_f32 v51, v51, v24, v25
	v_max3_f32 v52, v52, v46, v47
	s_nop 0
	v_max3_f32 v51, v51, v44, v45
	v_max3_f32 v52, v52, v30, v31
	s_nop 0
	v_max3_f32 v51, v51, v28, v29
	s_nop 0
	v_max_f32_e32 v51, v51, v52
	s_nop 0
	v_mov_b32_e32 v52, v51
	s_nop 1
	v_permlane32_swap_b32_e32 v51, v52
	v_max_f32_e32 v51, v51, v52
	s_nop 0
	v_add_f32_e32 v190, v181, v51
	v_sub_f32_e32 v52, v16, v51
	v_sub_f32_e32 v32, v32, v51
	v_sub_f32_e32 v33, v33, v51
	v_sub_f32_e32 v53, v17, v51
	v_sub_f32_e32 v34, v34, v51
	s_nop 0
	v_xor_b32_e32 v16, 0x80000000, v190
	v_sub_f32_e32 v54, v18, v51
	v_sub_f32_e32 v35, v35, v51
	v_sub_f32_e32 v55, v19, v51
	v_sub_f32_e32 v36, v36, v51
	v_sub_f32_e32 v56, v20, v51
	v_sub_f32_e32 v37, v37, v51
	v_sub_f32_e32 v57, v21, v51
	v_sub_f32_e32 v38, v38, v51
	v_sub_f32_e32 v58, v22, v51
	v_sub_f32_e32 v39, v39, v51
	v_sub_f32_e32 v59, v23, v51
	v_sub_f32_e32 v40, v40, v51
	v_sub_f32_e32 v60, v24, v51
	v_sub_f32_e32 v41, v41, v51
	v_sub_f32_e32 v61, v25, v51
	v_sub_f32_e32 v42, v42, v51
	v_sub_f32_e32 v62, v26, v51
	v_sub_f32_e32 v43, v43, v51
	v_sub_f32_e32 v63, v27, v51
	v_sub_f32_e32 v44, v44, v51
	v_sub_f32_e32 v64, v28, v51
	v_sub_f32_e32 v45, v45, v51
	v_sub_f32_e32 v65, v29, v51
	v_sub_f32_e32 v46, v46, v51
	v_sub_f32_e32 v66, v30, v51
	v_sub_f32_e32 v47, v47, v51
	v_sub_f32_e32 v51, v31, v51
	v_mov_b32_e32 v17, v16
	v_mov_b32_e32 v18, v16
	v_mov_b32_e32 v19, v16
	v_mov_b32_e32 v20, v16
	v_mov_b32_e32 v21, v16
	v_mov_b32_e32 v22, v16
	v_mov_b32_e32 v23, v16
	v_mov_b32_e32 v24, v16
	v_mov_b32_e32 v25, v16
	v_mov_b32_e32 v26, v16
	v_mov_b32_e32 v27, v16
	v_mov_b32_e32 v28, v16
	v_mov_b32_e32 v29, v16
	v_mov_b32_e32 v30, v16
	v_mov_b32_e32 v31, v16
	s_waitcnt vmcnt(0) lgkmcnt(0)
	s_barrier
; #define WAIT_BAR(N) asm volatile("s_waitcnt vmcnt(" #N ") lgkmcnt(0)\n\ts_barrier":::"memory")
;   #define DMA_K(t,slot) glds16(ksrc+(long)(t)*KVBLK*KP,(unsigned)__builtin_amdgcn_readfirstlane(kdst+(slot)))
;   #define DMA_V(t,slot) glds16(vsrc+(long)(t)*KVBLK*KP,(unsigned)__builtin_amdgcn_readfirstlane(vdst+(slot)))
;   #define CMASK(P0,P1,t) do{}while(0)
;   #define START(P0,P1) do{ const float rm=rowmax(P0,P1); resc=false; \
;     { const float dl=rm; mhat=fadd_s(mhat,dl); \
;       _Pragma("unroll") for(int r=0;r<16;++r){P0[r]=fsub_s(P0[r],dl);P1[r]=fsub_s(P1[r],dl);} \
;       _Pragma("unroll") for(int r=0;r<16;++r)negm[r]=-mhat; asm volatile("":"+v"(negm)); } \
;     _Pragma("unroll") for(int r=0;r<16;++r)P0[r]=__builtin_amdgcn_exp2f(P0[r]); }while(0)
;   #define ROT() do{sl_prev=sl_cur;sl_cur=sl_next;sl_next=(sl_next==(NSLOT-1)*SLOTB)?0:sl_next+SLOTB;}while(0)
; template<int THRL> __device__ __forceinline__ void attn_unit(long qrow0,int qcol,long kvrow0,int kvcol,int NT,long orow0,int ocol,const bf16*Q,const bf16* K,const bf16* V,bf16*O,char*shm,int wave_){
;     ...
;   qkt(pA0,pA1,Kbase,qr,negm,r32,hi);asm volatile("s_nop 15\n\ts_nop 7":"+v"(pA0),"+v"(pA1));CMASK(pA0,pA1,0);
;   START(pA0,pA1);
;   _Pragma("unroll") for(int r=0;r<16;++r)pA1[r]=__builtin_amdgcn_exp2f(pA1[r]);
;   WAIT_BAR(0);
;   DMA_K(3,0);DMA_V(1,SLOTB);
;   ROT();
;   kload8(kf,kp0+sl_cur);
;   WAIT_BAR(2);
;   s16x4 vlo[8],vhi[8]; u32x4 pw0,pw1,pw2,pw3;
	v_exp_f32_e32 v67, v32
	v_exp_f32_e32 v68, v33
	v_lshl_add_u64 v[32:33], v[48:49], 0, s[2:3]
	s_mov_b32 s1, m0
	s_mov_b32 m0, s0
	s_nop 0
	global_load_lds_dwordx4 v[32:33], off
	s_mov_b32 m0, s1
	v_lshl_add_u64 v[32:33], v[184:185], 0, s[22:23]
	s_add_i32 s0, s19, 0x2000
	s_mov_b32 s1, m0
	s_mov_b32 m0, s0
	s_nop 0
	global_load_lds_dwordx4 v[32:33], off
	s_mov_b32 m0, s1
	v_exp_f32_e32 v69, v34
	v_exp_f32_e32 v70, v35
	v_exp_f32_e32 v71, v36
	v_exp_f32_e32 v72, v37
	v_exp_f32_e32 v120, v38
	v_exp_f32_e32 v121, v39
	v_exp_f32_e32 v122, v40
	v_exp_f32_e32 v123, v41
	v_exp_f32_e32 v128, v42
	v_exp_f32_e32 v129, v43
	v_exp_f32_e32 v130, v44
	v_exp_f32_e32 v131, v45
	v_exp_f32_e32 v132, v46
	v_exp_f32_e32 v133, v47
	v_exp_f32_e32 v155, v60
	v_exp_f32_e32 v156, v61
	v_exp_f32_e32 v157, v62
	v_exp_f32_e32 v158, v63
	ds_read_b128 v[32:35], v194 offset:8192
	ds_read_b128 v[36:39], v194 offset:8704
	ds_read_b128 v[40:43], v194 offset:10240
	ds_read_b128 v[44:47], v194 offset:10752
	ds_read_b128 v[60:63], v194 offset:12288
	ds_read_b128 v[88:91], v194 offset:12800
	ds_read_b128 v[92:95], v194 offset:14336
	ds_read_b128 v[146:149], v194 offset:14848
	v_exp_f32_e32 v134, v52
	v_exp_f32_e32 v135, v53
	s_waitcnt vmcnt(2) lgkmcnt(0)
	s_barrier
	v_exp_f32_e32 v145, v54
	v_exp_f32_e32 v150, v55
	v_exp_f32_e32 v151, v56
	v_exp_f32_e32 v152, v57
	v_exp_f32_e32 v153, v58
	v_exp_f32_e32 v154, v59
	v_exp_f32_e32 v159, v64
	v_exp_f32_e32 v160, v65
	v_exp_f32_e32 v161, v66
	v_exp_f32_e32 v162, v51
	ds_read_b64_tr_b16 v[84:85], v193 offset:24576
	ds_read_b64_tr_b16 v[86:87], v193 offset:25088
	s_waitcnt lgkmcnt(9)
	v_mfma_f32_32x32x16_bf16 v[96:111], v[32:35], v[140:143], v[16:31]
	v_add_f32_e32 v48, v67, v68
	v_add_f32_e32 v48, v48, v69
	v_add_f32_e32 v48, v48, v70
	v_add_f32_e32 v48, v48, v71
	v_add_f32_e32 v48, v48, v72
	v_cvt_pk_bf16_f32 v124, v67, v68
	v_cvt_pk_bf16_f32 v125, v69, v70
	ds_read_b64_tr_b16 v[80:81], v193 offset:28672
	ds_read_b64_tr_b16 v[82:83], v193 offset:29184
	v_cvt_pk_bf16_f32 v126, v71, v72
	s_waitcnt lgkmcnt(10)
	v_mfma_f32_32x32x16_bf16 v[64:79], v[36:39], v[140:143], v[16:31]
	v_add_f32_e32 v32, v120, v48
	v_add_f32_e32 v32, v121, v32
	v_add_f32_e32 v32, v122, v32
	v_add_f32_e32 v32, v123, v32
	v_cvt_pk_bf16_f32 v127, v120, v121
	ds_read_b64_tr_b16 v[48:49], v193 offset:25600
	ds_read_b64_tr_b16 v[50:51], v193 offset:26112
	s_waitcnt lgkmcnt(11)
	v_mfma_f32_32x32x16_bf16 v[96:111], v[40:43], v[136:139], v[96:111]
	v_add_f32_e32 v32, v128, v32
	v_add_f32_e32 v32, v129, v32
	v_add_f32_e32 v32, v130, v32
	v_add_f32_e32 v32, v131, v32
	v_cvt_pk_bf16_f32 v120, v122, v123
	v_cvt_pk_bf16_f32 v121, v128, v129
	ds_read_b64_tr_b16 v[52:53], v193 offset:29696
	ds_read_b64_tr_b16 v[54:55], v193 offset:30208
	s_waitcnt lgkmcnt(12)
	v_mfma_f32_32x32x16_bf16 v[64:79], v[44:47], v[136:139], v[64:79]
	v_add_f32_e32 v32, v132, v32
	v_add_f32_e32 v32, v133, v32
	v_add_f32_e32 v32, v134, v32
	v_add_f32_e32 v32, v135, v32
	v_cvt_pk_bf16_f32 v122, v130, v131
	v_cvt_pk_bf16_f32 v123, v132, v133
	ds_read_b64_tr_b16 v[56:57], v193 offset:26624
	ds_read_b64_tr_b16 v[58:59], v193 offset:27136
	s_waitcnt lgkmcnt(13)
	v_mfma_f32_32x32x16_bf16 v[96:111], v[60:63], v[116:119], v[96:111]
	v_add_f32_e32 v32, v145, v32
	v_add_f32_e32 v32, v150, v32
	v_add_f32_e32 v32, v151, v32
	v_add_f32_e32 v32, v152, v32
	v_cvt_pk_bf16_f32 v128, v134, v135
	v_cvt_pk_bf16_f32 v129, v145, v150
	ds_read_b64_tr_b16 v[60:61], v193 offset:30720
	ds_read_b64_tr_b16 v[62:63], v193 offset:31232
	s_waitcnt lgkmcnt(14)
	v_mfma_f32_32x32x16_bf16 v[64:79], v[88:91], v[116:119], v[64:79]
	v_add_f32_e32 v32, v153, v32
	v_add_f32_e32 v32, v154, v32
	v_add_f32_e32 v32, v155, v32
	v_add_f32_e32 v32, v156, v32
	v_cvt_pk_bf16_f32 v130, v151, v152
	v_cvt_pk_bf16_f32 v131, v153, v154
	ds_read_b64_tr_b16 v[88:89], v193 offset:27648
	ds_read_b64_tr_b16 v[90:91], v193 offset:28160
	s_waitcnt lgkmcnt(14)
	v_mfma_f32_32x32x16_bf16 v[96:111], v[92:95], v[112:115], v[96:111]
	v_add_f32_e32 v32, v157, v32
	v_add_f32_e32 v32, v158, v32
	v_add_f32_e32 v32, v159, v32
	v_add_f32_e32 v32, v160, v32
	v_cvt_pk_bf16_f32 v132, v155, v156
	v_cvt_pk_bf16_f32 v133, v157, v158
	ds_read_b64_tr_b16 v[92:93], v193 offset:31744
	ds_read_b64_tr_b16 v[94:95], v193 offset:32256
	v_mfma_f32_32x32x16_bf16 v[64:79], v[146:149], v[112:115], v[64:79]
	v_add_f32_e32 v32, v161, v32
	v_add_f32_e32 v32, v162, v32
	v_cvt_pk_bf16_f32 v134, v159, v160
	v_cvt_pk_bf16_f32 v135, v161, v162
	s_nop 0
	v_add_f32_e32 v195, 0, v32
	v_lshl_add_u64 v[32:33], v[184:185], 0, s[10:11]
	s_add_i32 s0, s19, 0x4000
	s_mov_b32 s1, m0
	s_mov_b32 m0, s0
	s_nop 0
	global_load_lds_dwordx4 v[32:33], off
	s_mov_b32 m0, s1
	v_max_f32_e32 v32, v96, v97
	s_nop 2
	v_max3_f32 v33, v98, v99, v65
	v_max3_f32 v32, v32, v64, v66
	v_max3_f32 v32, v32, v67, v100
	v_max3_f32 v33, v33, v102, v103
	v_max3_f32 v32, v32, v101, v68
	v_max3_f32 v33, v33, v70, v71
	v_max3_f32 v32, v32, v69, v104
	v_max3_f32 v33, v33, v106, v107
	v_max3_f32 v32, v32, v105, v72
	v_max3_f32 v33, v33, v74, v75
	v_max3_f32 v32, v32, v73, v108
	v_max3_f32 v33, v33, v110, v111
	v_max3_f32 v32, v32, v109, v76
	v_max3_f32 v33, v33, v78, v79
	v_max3_f32 v32, v32, v77, v33
	v_mov_b32_e32 v33, v32
	s_nop 1
	v_permlane32_swap_b32_e32 v32, v33
	v_max_f32_e32 v32, v32, v33
	v_cmp_lt_f32_e32 vcc, s33, v32
	s_cmp_lg_u64 vcc, 0
	s_cselect_b64 s[0:1], -1, 0
	s_cbranch_vccnz .LBB0_1069

.LBB0_1061:
	ds_read_b64_tr_b16 v[148:149], v193 offset:32768
	ds_read_b64_tr_b16 v[150:151], v193 offset:33280
	s_waitcnt lgkmcnt(9)
	v_mfma_f32_32x32x16_bf16 v[80:95], v[144:147], v[140:143], v[16:31]
	v_add_f32_e32 v48, v96, v97
	v_add_f32_e32 v48, v98, v48
	v_add_f32_e32 v48, v99, v48
	v_add_f32_e32 v48, v100, v48
	v_add_f32_e32 v48, v101, v48
	v_cvt_pk_bf16_f32 v124, v96, v97
	v_cvt_pk_bf16_f32 v125, v98, v99
	ds_read_b64_tr_b16 v[144:145], v193 offset:36864
	ds_read_b64_tr_b16 v[146:147], v193 offset:37376
	v_add_f32_e32 v48, v102, v48
	v_add_f32_e32 v48, v103, v48
	v_add_f32_e32 v48, v104, v48
	v_add_f32_e32 v120, v105, v48
	s_waitcnt lgkmcnt(10)
	v_mfma_f32_32x32x16_bf16 v[48:63], v[172:175], v[140:143], v[16:31]
	v_cvt_pk_bf16_f32 v126, v100, v101
	v_cvt_pk_bf16_f32 v127, v102, v103
	ds_read_b64_tr_b16 v[96:97], v193 offset:33792
	ds_read_b64_tr_b16 v[98:99], v193 offset:34304
	s_waitcnt lgkmcnt(11)
	v_mfma_f32_32x32x16_bf16 v[80:95], v[176:179], v[136:139], v[80:95]
	v_add_f32_e32 v100, v106, v120
	v_add_f32_e32 v100, v107, v100
	v_add_f32_e32 v100, v108, v100
	v_add_f32_e32 v128, v109, v100
	v_cvt_pk_bf16_f32 v120, v104, v105
	v_cvt_pk_bf16_f32 v121, v106, v107
	ds_read_b64_tr_b16 v[100:101], v193 offset:37888
	ds_read_b64_tr_b16 v[102:103], v193 offset:38400
	s_waitcnt lgkmcnt(12)
	v_mfma_f32_32x32x16_bf16 v[48:63], v[168:171], v[136:139], v[48:63]
	v_add_f32_e32 v104, v110, v128
	v_add_f32_e32 v104, v111, v104
	v_add_f32_e32 v104, v64, v104
	v_add_f32_e32 v128, v65, v104
	v_cvt_pk_bf16_f32 v122, v108, v109
	v_cvt_pk_bf16_f32 v123, v110, v111
	ds_read_b64_tr_b16 v[104:105], v193 offset:34816
	ds_read_b64_tr_b16 v[106:107], v193 offset:35328
	s_waitcnt lgkmcnt(13)
	v_mfma_f32_32x32x16_bf16 v[80:95], v[164:167], v[116:119], v[80:95]
	v_add_f32_e32 v108, v66, v128
	v_add_f32_e32 v108, v67, v108
	v_add_f32_e32 v108, v68, v108
	v_add_f32_e32 v108, v69, v108
	v_cvt_pk_bf16_f32 v128, v64, v65
	v_cvt_pk_bf16_f32 v129, v66, v67
	ds_read_b64_tr_b16 v[64:65], v193 offset:38912
	ds_read_b64_tr_b16 v[66:67], v193 offset:39424
	s_waitcnt lgkmcnt(14)
	v_mfma_f32_32x32x16_bf16 v[48:63], v[160:163], v[116:119], v[48:63]
	v_add_f32_e32 v108, v70, v108
	v_add_f32_e32 v108, v71, v108
	v_add_f32_e32 v108, v72, v108
	v_add_f32_e32 v108, v73, v108
	v_cvt_pk_bf16_f32 v130, v68, v69
	v_cvt_pk_bf16_f32 v131, v70, v71
	ds_read_b64_tr_b16 v[68:69], v193 offset:35840
	ds_read_b64_tr_b16 v[70:71], v193 offset:36352
	s_waitcnt lgkmcnt(14)
	v_mfma_f32_32x32x16_bf16 v[80:95], v[156:159], v[112:115], v[80:95]
	v_add_f32_e32 v108, v74, v108
	v_add_f32_e32 v108, v75, v108
	v_add_f32_e32 v108, v76, v108
	v_add_f32_e32 v108, v77, v108
	v_cvt_pk_bf16_f32 v132, v72, v73
	v_cvt_pk_bf16_f32 v133, v74, v75
	ds_read_b64_tr_b16 v[72:73], v193 offset:39936
	ds_read_b64_tr_b16 v[74:75], v193 offset:40448
	v_mfma_f32_32x32x16_bf16 v[48:63], v[152:155], v[112:115], v[48:63]
	v_add_f32_e32 v108, v78, v108
	v_add_f32_e32 v108, v79, v108
	v_cvt_pk_bf16_f32 v134, v76, v77
	v_cvt_pk_bf16_f32 v135, v78, v79
	s_mov_b64 s[0:1], 0xc000
	v_lshl_add_u64 v[76:77], v[184:185], 0, s[0:1]
	s_mov_b32 s0, m0
	s_mov_b32 m0, s19
	s_nop 0
	global_load_lds_dwordx4 v[76:77], off
	s_mov_b32 m0, s0
	v_max_f32_e32 v76, v80, v81
	s_nop 1
	s_nop 2
	v_max3_f32 v77, v82, v83, v49
	v_max3_f32 v76, v76, v48, v50
	v_max3_f32 v76, v76, v51, v84
	v_max3_f32 v77, v77, v86, v87
	v_max3_f32 v76, v76, v85, v52
	v_max3_f32 v77, v77, v54, v55
	v_max3_f32 v76, v76, v53, v88
	v_max3_f32 v77, v77, v90, v91
	v_max3_f32 v76, v76, v89, v56
	v_max3_f32 v77, v77, v58, v59
	v_max3_f32 v76, v76, v57, v92
	v_max3_f32 v77, v77, v94, v95
	v_max3_f32 v76, v76, v93, v60
	v_max3_f32 v77, v77, v62, v63
	v_max3_f32 v76, v76, v61, v77
	v_mov_b32_e32 v77, v76
	s_nop 1
	v_permlane32_swap_b32_e32 v76, v77
	v_max_f32_e32 v76, v76, v77
	v_cmp_lt_f32_e32 vcc, s33, v76
	s_cmp_lg_u64 vcc, 0
	v_add_f32_e32 v168, v195, v108
	s_cselect_b64 s[0:1], -1, 0
	s_cbranch_vccnz .LBB0_1072

.LBB0_1064:
	ds_read_b64_tr_b16 v[96:97], v193 offset:40960
	ds_read_b64_tr_b16 v[98:99], v193 offset:41472
	v_add_f32_e32 v64, v80, v81
	v_add_f32_e32 v64, v82, v64
	v_add_f32_e32 v64, v83, v64
	v_add_f32_e32 v64, v84, v64
	v_add_f32_e32 v104, v85, v64
	s_waitcnt lgkmcnt(9)
	v_mfma_f32_32x32x16_bf16 v[64:79], v[164:167], v[140:143], v[16:31]
	v_cvt_pk_bf16_f32 v124, v80, v81
	v_cvt_pk_bf16_f32 v125, v82, v83
	ds_read_b64_tr_b16 v[80:81], v193 offset:45056
	ds_read_b64_tr_b16 v[82:83], v193 offset:45568
	s_waitcnt lgkmcnt(10)
	v_mfma_f32_32x32x16_bf16 v[16:31], v[160:163], v[140:143], v[16:31]
	v_add_f32_e32 v104, v86, v104
	v_add_f32_e32 v104, v87, v104
	v_add_f32_e32 v104, v88, v104
	v_add_f32_e32 v104, v89, v104
	v_cvt_pk_bf16_f32 v126, v84, v85
	v_cvt_pk_bf16_f32 v127, v86, v87
	ds_read_b64_tr_b16 v[84:85], v193 offset:41984
	ds_read_b64_tr_b16 v[86:87], v193 offset:42496
	s_waitcnt lgkmcnt(11)
	v_mfma_f32_32x32x16_bf16 v[64:79], v[156:159], v[136:139], v[64:79]
	v_add_f32_e32 v104, v90, v104
	v_add_f32_e32 v104, v91, v104
	v_add_f32_e32 v104, v92, v104
	v_add_f32_e32 v104, v93, v104
	v_cvt_pk_bf16_f32 v120, v88, v89
	v_cvt_pk_bf16_f32 v121, v90, v91
	ds_read_b64_tr_b16 v[88:89], v193 offset:46080
	ds_read_b64_tr_b16 v[90:91], v193 offset:46592
	s_waitcnt lgkmcnt(12)
	v_mfma_f32_32x32x16_bf16 v[16:31], v[152:155], v[136:139], v[16:31]
	v_add_f32_e32 v104, v94, v104
	v_add_f32_e32 v104, v95, v104
	v_add_f32_e32 v104, v48, v104
	v_add_f32_e32 v104, v49, v104
	v_cvt_pk_bf16_f32 v122, v92, v93
	v_cvt_pk_bf16_f32 v123, v94, v95
	ds_read_b64_tr_b16 v[92:93], v193 offset:43008
	ds_read_b64_tr_b16 v[94:95], v193 offset:43520
	s_waitcnt lgkmcnt(13)
	v_mfma_f32_32x32x16_bf16 v[64:79], v[100:103], v[116:119], v[64:79]
	v_add_f32_e32 v100, v50, v104
	v_add_f32_e32 v100, v51, v100
	v_add_f32_e32 v100, v52, v100
	v_add_f32_e32 v104, v53, v100
	v_cvt_pk_bf16_f32 v128, v48, v49
	v_cvt_pk_bf16_f32 v129, v50, v51
	ds_read_b64_tr_b16 v[100:101], v193 offset:47104
	ds_read_b64_tr_b16 v[102:103], v193 offset:47616
	s_waitcnt lgkmcnt(14)
	v_mfma_f32_32x32x16_bf16 v[16:31], v[148:151], v[116:119], v[16:31]
	v_add_f32_e32 v48, v54, v104
	v_add_f32_e32 v48, v55, v48
	v_add_f32_e32 v48, v56, v48
	v_add_f32_e32 v48, v57, v48
	v_cvt_pk_bf16_f32 v130, v52, v53
	v_cvt_pk_bf16_f32 v131, v54, v55
	ds_read_b64_tr_b16 v[104:105], v193 offset:44032
	ds_read_b64_tr_b16 v[106:107], v193 offset:44544
	s_waitcnt lgkmcnt(14)
	v_mfma_f32_32x32x16_bf16 v[64:79], v[144:147], v[112:115], v[64:79]
	v_add_f32_e32 v48, v58, v48
	v_add_f32_e32 v48, v59, v48
	v_add_f32_e32 v48, v60, v48
	v_add_f32_e32 v48, v61, v48
	v_cvt_pk_bf16_f32 v132, v56, v57
	v_cvt_pk_bf16_f32 v133, v58, v59
	ds_read_b64_tr_b16 v[116:117], v193 offset:48128
	ds_read_b64_tr_b16 v[118:119], v193 offset:48640
	v_mfma_f32_32x32x16_bf16 v[16:31], v[108:111], v[112:115], v[16:31]
	v_add_f32_e32 v48, v62, v48
	v_add_f32_e32 v48, v63, v48
	v_cvt_pk_bf16_f32 v134, v60, v61
	v_cvt_pk_bf16_f32 v135, v62, v63
	v_max_f32_e32 v49, v64, v65
	s_nop 3
	s_nop 2
	v_max3_f32 v50, v66, v67, v17
	v_max3_f32 v49, v49, v16, v18
	v_max3_f32 v49, v49, v19, v68
	v_max3_f32 v50, v50, v70, v71
	v_max3_f32 v49, v49, v69, v20
	v_max3_f32 v50, v50, v22, v23
	v_max3_f32 v49, v49, v21, v72
	v_max3_f32 v50, v50, v74, v75
	v_max3_f32 v49, v49, v73, v24
	v_max3_f32 v50, v50, v26, v27
	v_max3_f32 v49, v49, v25, v76
	v_max3_f32 v50, v50, v78, v79
	v_max3_f32 v49, v49, v77, v28
	v_max3_f32 v50, v50, v30, v31
	v_add_f32_e32 v108, v168, v48
	v_max3_f32 v48, v49, v29, v50
	v_mov_b32_e32 v49, v48
	s_nop 1
	v_permlane32_swap_b32_e32 v48, v49
	v_max_f32_e32 v48, v48, v49
	v_cmp_lt_f32_e32 vcc, s33, v48
	s_cmp_lg_u64 vcc, 0
	s_cselect_b64 s[0:1], -1, 0
	s_cbranch_vccnz .LBB0_1075
